# P7 epilogue: 64 byte stores per lane -> per row one packed dword (4 e4m3), 4x4 byte transpose inside lane quads (DPP quad_perm + v_perm_b32), 16 global_store_dword per lane; placement of later code ke
# speedup vs baseline: 1.0057x; 1.0057x over previous
.LBB0_1720:
	s_or_b64 exec, exec, s[6:7]
	s_waitcnt lgkmcnt(0)
	s_mov_b64 s[26:27], 0
	ds_read_b128 v[120:123], v198
	ds_read_b128 v[124:127], v198 offset:32
	ds_read_b128 v[128:131], v198 offset:64
	ds_read_b128 v[132:135], v198 offset:96
	v_and_b32_e32 v86, 3, v0
	v_mul_u32_u24_e32 v136, 0x101, v86
	v_add_u32_e32 v136, 0xc0c0400, v136
	v_mul_u32_u24_e32 v86, 31, v86
	v_mov_b32_e32 v87, 0
	v_lshl_add_u64 v[74:75], v[178:179], 0, s[24:25]
	v_lshlrev_b32_e32 v137, 16, v136
	v_or_b32_e32 v137, 0xc0c, v137
	v_lshl_add_u64 v[74:75], v[74:75], 0, v[86:87]
	v_add_co_u32_e32 v76, vcc, s41, v74
	s_nop 1
	v_addc_co_u32_e32 v77, vcc, 0, v75, vcc
	v_add_co_u32_e32 v78, vcc, s30, v74
	s_nop 1
	v_addc_co_u32_e32 v79, vcc, 0, v75, vcc
	v_add_co_u32_e32 v80, vcc, s42, v74
	s_nop 1
	v_addc_co_u32_e32 v81, vcc, 0, v75, vcc
	s_waitcnt lgkmcnt(3)
	v_rcp_f32_e32 v104, v120
	v_rcp_f32_e32 v105, v121
	v_rcp_f32_e32 v106, v122
	v_rcp_f32_e32 v107, v123
	s_waitcnt lgkmcnt(2)
	v_rcp_f32_e32 v108, v124
	v_rcp_f32_e32 v109, v125
	v_rcp_f32_e32 v110, v126
	v_rcp_f32_e32 v111, v127
	s_waitcnt lgkmcnt(1)
	v_rcp_f32_e32 v112, v128
	v_rcp_f32_e32 v113, v129
	v_rcp_f32_e32 v114, v130
	v_rcp_f32_e32 v115, v131
	s_waitcnt lgkmcnt(0)
	v_rcp_f32_e32 v116, v132
	v_rcp_f32_e32 v117, v133
	v_rcp_f32_e32 v118, v134
	v_rcp_f32_e32 v119, v135
	s_nop 0
	v_mul_f32_e32 v138, v50, v104
	v_mul_f32_e32 v139, v34, v104
	v_mul_f32_e32 v140, v18, v104
	v_mul_f32_e32 v141, v2, v104
	v_mul_f32_e32 v138, 0x42000000, v138
	v_mul_f32_e32 v139, 0x42000000, v139
	v_mul_f32_e32 v140, 0x42000000, v140
	v_mul_f32_e32 v141, 0x42000000, v141
	v_med3_f32 v138, v138, s40, v212
	v_med3_f32 v139, v139, s40, v212
	v_med3_f32 v140, v140, s40, v212
	v_med3_f32 v141, v141, s40, v212
	v_cvt_pk_fp8_f32 v142, v138, v139
	v_cvt_pk_fp8_f32 v142, v140, v141 op_sel:[0,0,1]
	v_mul_f32_e32 v138, v51, v105
	v_mul_f32_e32 v139, v35, v105
	v_mul_f32_e32 v140, v19, v105
	v_mul_f32_e32 v141, v3, v105
	v_mul_f32_e32 v138, 0x42000000, v138
	v_mul_f32_e32 v139, 0x42000000, v139
	v_mul_f32_e32 v140, 0x42000000, v140
	v_mul_f32_e32 v141, 0x42000000, v141
	v_med3_f32 v138, v138, s40, v212
	v_med3_f32 v139, v139, s40, v212
	v_med3_f32 v140, v140, s40, v212
	v_med3_f32 v141, v141, s40, v212
	v_cvt_pk_fp8_f32 v143, v138, v139
	v_cvt_pk_fp8_f32 v143, v140, v141 op_sel:[0,0,1]
	v_mov_b32_dpp v66, v142 quad_perm:[0,0,0,0] row_mask:0xf bank_mask:0xf
	v_mov_b32_dpp v67, v142 quad_perm:[1,1,1,1] row_mask:0xf bank_mask:0xf
	v_mov_b32_dpp v68, v142 quad_perm:[2,2,2,2] row_mask:0xf bank_mask:0xf
	v_mov_b32_dpp v69, v142 quad_perm:[3,3,3,3] row_mask:0xf bank_mask:0xf
	s_nop 0
	v_perm_b32 v70, v67, v66, v136
	v_perm_b32 v71, v69, v68, v137
	v_or_b32_e32 v72, v70, v71
	global_store_dword v[74:75], v72, off
	v_mul_f32_e32 v138, v52, v106
	v_mul_f32_e32 v139, v36, v106
	v_mul_f32_e32 v140, v20, v106
	v_mul_f32_e32 v141, v4, v106
	v_mul_f32_e32 v138, 0x42000000, v138
	v_mul_f32_e32 v139, 0x42000000, v139
	v_mul_f32_e32 v140, 0x42000000, v140
	v_mul_f32_e32 v141, 0x42000000, v141
	v_med3_f32 v138, v138, s40, v212
	v_med3_f32 v139, v139, s40, v212
	v_med3_f32 v140, v140, s40, v212
	v_med3_f32 v141, v141, s40, v212
	v_cvt_pk_fp8_f32 v142, v138, v139
	v_cvt_pk_fp8_f32 v142, v140, v141 op_sel:[0,0,1]
	v_mov_b32_dpp v66, v143 quad_perm:[0,0,0,0] row_mask:0xf bank_mask:0xf
	v_mov_b32_dpp v67, v143 quad_perm:[1,1,1,1] row_mask:0xf bank_mask:0xf
	v_mov_b32_dpp v68, v143 quad_perm:[2,2,2,2] row_mask:0xf bank_mask:0xf
	v_mov_b32_dpp v69, v143 quad_perm:[3,3,3,3] row_mask:0xf bank_mask:0xf
	s_nop 0
	v_perm_b32 v70, v67, v66, v136
	v_perm_b32 v71, v69, v68, v137
	v_or_b32_e32 v72, v70, v71
	global_store_dword v[74:75], v72, off offset:1024
	v_mul_f32_e32 v138, v53, v107
	v_mul_f32_e32 v139, v37, v107
	v_mul_f32_e32 v140, v21, v107
	v_mul_f32_e32 v141, v5, v107
	v_mul_f32_e32 v138, 0x42000000, v138
	v_mul_f32_e32 v139, 0x42000000, v139
	v_mul_f32_e32 v140, 0x42000000, v140
	v_mul_f32_e32 v141, 0x42000000, v141
	v_med3_f32 v138, v138, s40, v212
	v_med3_f32 v139, v139, s40, v212
	v_med3_f32 v140, v140, s40, v212
	v_med3_f32 v141, v141, s40, v212
	v_cvt_pk_fp8_f32 v143, v138, v139
	v_cvt_pk_fp8_f32 v143, v140, v141 op_sel:[0,0,1]
	v_mov_b32_dpp v66, v142 quad_perm:[0,0,0,0] row_mask:0xf bank_mask:0xf
	v_mov_b32_dpp v67, v142 quad_perm:[1,1,1,1] row_mask:0xf bank_mask:0xf
	v_mov_b32_dpp v68, v142 quad_perm:[2,2,2,2] row_mask:0xf bank_mask:0xf
	v_mov_b32_dpp v69, v142 quad_perm:[3,3,3,3] row_mask:0xf bank_mask:0xf
	s_nop 0
	v_perm_b32 v70, v67, v66, v136
	v_perm_b32 v71, v69, v68, v137
	v_or_b32_e32 v72, v70, v71
	global_store_dword v[74:75], v72, off offset:2048
	v_mul_f32_e32 v138, v54, v108
	v_mul_f32_e32 v139, v38, v108
	v_mul_f32_e32 v140, v22, v108
	v_mul_f32_e32 v141, v6, v108
	v_mul_f32_e32 v138, 0x42000000, v138
	v_mul_f32_e32 v139, 0x42000000, v139
	v_mul_f32_e32 v140, 0x42000000, v140
	v_mul_f32_e32 v141, 0x42000000, v141
	v_med3_f32 v138, v138, s40, v212
	v_med3_f32 v139, v139, s40, v212
	v_med3_f32 v140, v140, s40, v212
	v_med3_f32 v141, v141, s40, v212
	v_cvt_pk_fp8_f32 v142, v138, v139
	v_cvt_pk_fp8_f32 v142, v140, v141 op_sel:[0,0,1]
	v_mov_b32_dpp v66, v143 quad_perm:[0,0,0,0] row_mask:0xf bank_mask:0xf
	v_mov_b32_dpp v67, v143 quad_perm:[1,1,1,1] row_mask:0xf bank_mask:0xf
	v_mov_b32_dpp v68, v143 quad_perm:[2,2,2,2] row_mask:0xf bank_mask:0xf
	v_mov_b32_dpp v69, v143 quad_perm:[3,3,3,3] row_mask:0xf bank_mask:0xf
	s_nop 0
	v_perm_b32 v70, v67, v66, v136
	v_perm_b32 v71, v69, v68, v137
	v_or_b32_e32 v72, v70, v71
	global_store_dword v[74:75], v72, off offset:3072
	v_mul_f32_e32 v138, v55, v109
	v_mul_f32_e32 v139, v39, v109
	v_mul_f32_e32 v140, v23, v109
	v_mul_f32_e32 v141, v7, v109
	v_mul_f32_e32 v138, 0x42000000, v138
	v_mul_f32_e32 v139, 0x42000000, v139
	v_mul_f32_e32 v140, 0x42000000, v140
	v_mul_f32_e32 v141, 0x42000000, v141
	v_med3_f32 v138, v138, s40, v212
	v_med3_f32 v139, v139, s40, v212
	v_med3_f32 v140, v140, s40, v212
	v_med3_f32 v141, v141, s40, v212
	v_cvt_pk_fp8_f32 v143, v138, v139
	v_cvt_pk_fp8_f32 v143, v140, v141 op_sel:[0,0,1]
	v_mov_b32_dpp v66, v142 quad_perm:[0,0,0,0] row_mask:0xf bank_mask:0xf
	v_mov_b32_dpp v67, v142 quad_perm:[1,1,1,1] row_mask:0xf bank_mask:0xf
	v_mov_b32_dpp v68, v142 quad_perm:[2,2,2,2] row_mask:0xf bank_mask:0xf
	v_mov_b32_dpp v69, v142 quad_perm:[3,3,3,3] row_mask:0xf bank_mask:0xf
	s_nop 0
	v_perm_b32 v70, v67, v66, v136
	v_perm_b32 v71, v69, v68, v137
	v_or_b32_e32 v72, v70, v71
	global_store_dword v[76:77], v72, off
	v_mul_f32_e32 v138, v56, v110
	v_mul_f32_e32 v139, v40, v110
	v_mul_f32_e32 v140, v24, v110
	v_mul_f32_e32 v141, v8, v110
	v_mul_f32_e32 v138, 0x42000000, v138
	v_mul_f32_e32 v139, 0x42000000, v139
	v_mul_f32_e32 v140, 0x42000000, v140
	v_mul_f32_e32 v141, 0x42000000, v141
	v_med3_f32 v138, v138, s40, v212
	v_med3_f32 v139, v139, s40, v212
	v_med3_f32 v140, v140, s40, v212
	v_med3_f32 v141, v141, s40, v212
	v_cvt_pk_fp8_f32 v142, v138, v139
	v_cvt_pk_fp8_f32 v142, v140, v141 op_sel:[0,0,1]
	v_mov_b32_dpp v66, v143 quad_perm:[0,0,0,0] row_mask:0xf bank_mask:0xf
	v_mov_b32_dpp v67, v143 quad_perm:[1,1,1,1] row_mask:0xf bank_mask:0xf
	v_mov_b32_dpp v68, v143 quad_perm:[2,2,2,2] row_mask:0xf bank_mask:0xf
	v_mov_b32_dpp v69, v143 quad_perm:[3,3,3,3] row_mask:0xf bank_mask:0xf
	s_nop 0
	v_perm_b32 v70, v67, v66, v136
	v_perm_b32 v71, v69, v68, v137
	v_or_b32_e32 v72, v70, v71
	global_store_dword v[76:77], v72, off offset:1024
	v_mul_f32_e32 v138, v57, v111
	v_mul_f32_e32 v139, v41, v111
	v_mul_f32_e32 v140, v25, v111
	v_mul_f32_e32 v141, v9, v111
	v_mul_f32_e32 v138, 0x42000000, v138
	v_mul_f32_e32 v139, 0x42000000, v139
	v_mul_f32_e32 v140, 0x42000000, v140
	v_mul_f32_e32 v141, 0x42000000, v141
	v_med3_f32 v138, v138, s40, v212
	v_med3_f32 v139, v139, s40, v212
	v_med3_f32 v140, v140, s40, v212
	v_med3_f32 v141, v141, s40, v212
	v_cvt_pk_fp8_f32 v143, v138, v139
	v_cvt_pk_fp8_f32 v143, v140, v141 op_sel:[0,0,1]
	v_mov_b32_dpp v66, v142 quad_perm:[0,0,0,0] row_mask:0xf bank_mask:0xf
	v_mov_b32_dpp v67, v142 quad_perm:[1,1,1,1] row_mask:0xf bank_mask:0xf
	v_mov_b32_dpp v68, v142 quad_perm:[2,2,2,2] row_mask:0xf bank_mask:0xf
	v_mov_b32_dpp v69, v142 quad_perm:[3,3,3,3] row_mask:0xf bank_mask:0xf
	s_nop 0
	v_perm_b32 v70, v67, v66, v136
	v_perm_b32 v71, v69, v68, v137
	v_or_b32_e32 v72, v70, v71
	global_store_dword v[76:77], v72, off offset:2048
	v_mul_f32_e32 v138, v58, v112
	v_mul_f32_e32 v139, v42, v112
	v_mul_f32_e32 v140, v26, v112
	v_mul_f32_e32 v141, v10, v112
	v_mul_f32_e32 v138, 0x42000000, v138
	v_mul_f32_e32 v139, 0x42000000, v139
	v_mul_f32_e32 v140, 0x42000000, v140
	v_mul_f32_e32 v141, 0x42000000, v141
	v_med3_f32 v138, v138, s40, v212
	v_med3_f32 v139, v139, s40, v212
	v_med3_f32 v140, v140, s40, v212
	v_med3_f32 v141, v141, s40, v212
	v_cvt_pk_fp8_f32 v142, v138, v139
	v_cvt_pk_fp8_f32 v142, v140, v141 op_sel:[0,0,1]
	v_mov_b32_dpp v66, v143 quad_perm:[0,0,0,0] row_mask:0xf bank_mask:0xf
	v_mov_b32_dpp v67, v143 quad_perm:[1,1,1,1] row_mask:0xf bank_mask:0xf
	v_mov_b32_dpp v68, v143 quad_perm:[2,2,2,2] row_mask:0xf bank_mask:0xf
	v_mov_b32_dpp v69, v143 quad_perm:[3,3,3,3] row_mask:0xf bank_mask:0xf
	s_nop 0
	v_perm_b32 v70, v67, v66, v136
	v_perm_b32 v71, v69, v68, v137
	v_or_b32_e32 v72, v70, v71
	global_store_dword v[76:77], v72, off offset:3072
	v_mul_f32_e32 v138, v59, v113
	v_mul_f32_e32 v139, v43, v113
	v_mul_f32_e32 v140, v27, v113
	v_mul_f32_e32 v141, v11, v113
	v_mul_f32_e32 v138, 0x42000000, v138
	v_mul_f32_e32 v139, 0x42000000, v139
	v_mul_f32_e32 v140, 0x42000000, v140
	v_mul_f32_e32 v141, 0x42000000, v141
	v_med3_f32 v138, v138, s40, v212
	v_med3_f32 v139, v139, s40, v212
	v_med3_f32 v140, v140, s40, v212
	v_med3_f32 v141, v141, s40, v212
	v_cvt_pk_fp8_f32 v143, v138, v139
	v_cvt_pk_fp8_f32 v143, v140, v141 op_sel:[0,0,1]
	v_mov_b32_dpp v66, v142 quad_perm:[0,0,0,0] row_mask:0xf bank_mask:0xf
	v_mov_b32_dpp v67, v142 quad_perm:[1,1,1,1] row_mask:0xf bank_mask:0xf
	v_mov_b32_dpp v68, v142 quad_perm:[2,2,2,2] row_mask:0xf bank_mask:0xf
	v_mov_b32_dpp v69, v142 quad_perm:[3,3,3,3] row_mask:0xf bank_mask:0xf
	s_nop 0
	v_perm_b32 v70, v67, v66, v136
	v_perm_b32 v71, v69, v68, v137
	v_or_b32_e32 v72, v70, v71
	global_store_dword v[78:79], v72, off
	v_mul_f32_e32 v138, v60, v114
	v_mul_f32_e32 v139, v44, v114
	v_mul_f32_e32 v140, v28, v114
	v_mul_f32_e32 v141, v12, v114
	v_mul_f32_e32 v138, 0x42000000, v138
	v_mul_f32_e32 v139, 0x42000000, v139
	v_mul_f32_e32 v140, 0x42000000, v140
	v_mul_f32_e32 v141, 0x42000000, v141
	v_med3_f32 v138, v138, s40, v212
	v_med3_f32 v139, v139, s40, v212
	v_med3_f32 v140, v140, s40, v212
	v_med3_f32 v141, v141, s40, v212
	v_cvt_pk_fp8_f32 v142, v138, v139
	v_cvt_pk_fp8_f32 v142, v140, v141 op_sel:[0,0,1]
	v_mov_b32_dpp v66, v143 quad_perm:[0,0,0,0] row_mask:0xf bank_mask:0xf
	v_mov_b32_dpp v67, v143 quad_perm:[1,1,1,1] row_mask:0xf bank_mask:0xf
	v_mov_b32_dpp v68, v143 quad_perm:[2,2,2,2] row_mask:0xf bank_mask:0xf
	v_mov_b32_dpp v69, v143 quad_perm:[3,3,3,3] row_mask:0xf bank_mask:0xf
	s_nop 0
	v_perm_b32 v70, v67, v66, v136
	v_perm_b32 v71, v69, v68, v137
	v_or_b32_e32 v72, v70, v71
	global_store_dword v[78:79], v72, off offset:1024
	v_mul_f32_e32 v138, v61, v115
	v_mul_f32_e32 v139, v45, v115
	v_mul_f32_e32 v140, v29, v115
	v_mul_f32_e32 v141, v13, v115
	v_mul_f32_e32 v138, 0x42000000, v138
	v_mul_f32_e32 v139, 0x42000000, v139
	v_mul_f32_e32 v140, 0x42000000, v140
	v_mul_f32_e32 v141, 0x42000000, v141
	v_med3_f32 v138, v138, s40, v212
	v_med3_f32 v139, v139, s40, v212
	v_med3_f32 v140, v140, s40, v212
	v_med3_f32 v141, v141, s40, v212
	v_cvt_pk_fp8_f32 v143, v138, v139
	v_cvt_pk_fp8_f32 v143, v140, v141 op_sel:[0,0,1]
	v_mov_b32_dpp v66, v142 quad_perm:[0,0,0,0] row_mask:0xf bank_mask:0xf
	v_mov_b32_dpp v67, v142 quad_perm:[1,1,1,1] row_mask:0xf bank_mask:0xf
	v_mov_b32_dpp v68, v142 quad_perm:[2,2,2,2] row_mask:0xf bank_mask:0xf
	v_mov_b32_dpp v69, v142 quad_perm:[3,3,3,3] row_mask:0xf bank_mask:0xf
	s_nop 0
	v_perm_b32 v70, v67, v66, v136
	v_perm_b32 v71, v69, v68, v137
	v_or_b32_e32 v72, v70, v71
	global_store_dword v[78:79], v72, off offset:2048
	v_mul_f32_e32 v138, v62, v116
	v_mul_f32_e32 v139, v46, v116
	v_mul_f32_e32 v140, v30, v116
	v_mul_f32_e32 v141, v14, v116
	v_mul_f32_e32 v138, 0x42000000, v138
	v_mul_f32_e32 v139, 0x42000000, v139
	v_mul_f32_e32 v140, 0x42000000, v140
	v_mul_f32_e32 v141, 0x42000000, v141
	v_med3_f32 v138, v138, s40, v212
	v_med3_f32 v139, v139, s40, v212
	v_med3_f32 v140, v140, s40, v212
	v_med3_f32 v141, v141, s40, v212
	v_cvt_pk_fp8_f32 v142, v138, v139
	v_cvt_pk_fp8_f32 v142, v140, v141 op_sel:[0,0,1]
	v_mov_b32_dpp v66, v143 quad_perm:[0,0,0,0] row_mask:0xf bank_mask:0xf
	v_mov_b32_dpp v67, v143 quad_perm:[1,1,1,1] row_mask:0xf bank_mask:0xf
	v_mov_b32_dpp v68, v143 quad_perm:[2,2,2,2] row_mask:0xf bank_mask:0xf
	v_mov_b32_dpp v69, v143 quad_perm:[3,3,3,3] row_mask:0xf bank_mask:0xf
	s_nop 0
	v_perm_b32 v70, v67, v66, v136
	v_perm_b32 v71, v69, v68, v137
	v_or_b32_e32 v72, v70, v71
	global_store_dword v[78:79], v72, off offset:3072
	v_mul_f32_e32 v138, v63, v117
	v_mul_f32_e32 v139, v47, v117
	v_mul_f32_e32 v140, v31, v117
	v_mul_f32_e32 v141, v15, v117
	v_mul_f32_e32 v138, 0x42000000, v138
	v_mul_f32_e32 v139, 0x42000000, v139
	v_mul_f32_e32 v140, 0x42000000, v140
	v_mul_f32_e32 v141, 0x42000000, v141
	v_med3_f32 v138, v138, s40, v212
	v_med3_f32 v139, v139, s40, v212
	v_med3_f32 v140, v140, s40, v212
	v_med3_f32 v141, v141, s40, v212
	v_cvt_pk_fp8_f32 v143, v138, v139
	v_cvt_pk_fp8_f32 v143, v140, v141 op_sel:[0,0,1]
	v_mov_b32_dpp v66, v142 quad_perm:[0,0,0,0] row_mask:0xf bank_mask:0xf
	v_mov_b32_dpp v67, v142 quad_perm:[1,1,1,1] row_mask:0xf bank_mask:0xf
	v_mov_b32_dpp v68, v142 quad_perm:[2,2,2,2] row_mask:0xf bank_mask:0xf
	v_mov_b32_dpp v69, v142 quad_perm:[3,3,3,3] row_mask:0xf bank_mask:0xf
	s_nop 0
	v_perm_b32 v70, v67, v66, v136
	v_perm_b32 v71, v69, v68, v137
	v_or_b32_e32 v72, v70, v71
	global_store_dword v[80:81], v72, off
	v_mul_f32_e32 v138, v64, v118
	v_mul_f32_e32 v139, v48, v118
	v_mul_f32_e32 v140, v32, v118
	v_mul_f32_e32 v141, v16, v118
	v_mul_f32_e32 v138, 0x42000000, v138
	v_mul_f32_e32 v139, 0x42000000, v139
	v_mul_f32_e32 v140, 0x42000000, v140
	v_mul_f32_e32 v141, 0x42000000, v141
	v_med3_f32 v138, v138, s40, v212
	v_med3_f32 v139, v139, s40, v212
	v_med3_f32 v140, v140, s40, v212
	v_med3_f32 v141, v141, s40, v212
	v_cvt_pk_fp8_f32 v142, v138, v139
	v_cvt_pk_fp8_f32 v142, v140, v141 op_sel:[0,0,1]
	v_mov_b32_dpp v66, v143 quad_perm:[0,0,0,0] row_mask:0xf bank_mask:0xf
	v_mov_b32_dpp v67, v143 quad_perm:[1,1,1,1] row_mask:0xf bank_mask:0xf
	v_mov_b32_dpp v68, v143 quad_perm:[2,2,2,2] row_mask:0xf bank_mask:0xf
	v_mov_b32_dpp v69, v143 quad_perm:[3,3,3,3] row_mask:0xf bank_mask:0xf
	s_nop 0
	v_perm_b32 v70, v67, v66, v136
	v_perm_b32 v71, v69, v68, v137
	v_or_b32_e32 v72, v70, v71
	global_store_dword v[80:81], v72, off offset:1024
	v_mul_f32_e32 v138, v65, v119
	v_mul_f32_e32 v139, v49, v119
	v_mul_f32_e32 v140, v33, v119
	v_mul_f32_e32 v141, v17, v119
	v_mul_f32_e32 v138, 0x42000000, v138
	v_mul_f32_e32 v139, 0x42000000, v139
	v_mul_f32_e32 v140, 0x42000000, v140
	v_mul_f32_e32 v141, 0x42000000, v141
	v_med3_f32 v138, v138, s40, v212
	v_med3_f32 v139, v139, s40, v212
	v_med3_f32 v140, v140, s40, v212
	v_med3_f32 v141, v141, s40, v212
	v_cvt_pk_fp8_f32 v143, v138, v139
	v_cvt_pk_fp8_f32 v143, v140, v141 op_sel:[0,0,1]
	v_mov_b32_dpp v66, v142 quad_perm:[0,0,0,0] row_mask:0xf bank_mask:0xf
	v_mov_b32_dpp v67, v142 quad_perm:[1,1,1,1] row_mask:0xf bank_mask:0xf
	v_mov_b32_dpp v68, v142 quad_perm:[2,2,2,2] row_mask:0xf bank_mask:0xf
	v_mov_b32_dpp v69, v142 quad_perm:[3,3,3,3] row_mask:0xf bank_mask:0xf
	s_nop 0
	v_perm_b32 v70, v67, v66, v136
	v_perm_b32 v71, v69, v68, v137
	v_or_b32_e32 v72, v70, v71
	global_store_dword v[80:81], v72, off offset:2048
	s_nop 1
	v_mov_b32_dpp v66, v143 quad_perm:[0,0,0,0] row_mask:0xf bank_mask:0xf
	v_mov_b32_dpp v67, v143 quad_perm:[1,1,1,1] row_mask:0xf bank_mask:0xf
	v_mov_b32_dpp v68, v143 quad_perm:[2,2,2,2] row_mask:0xf bank_mask:0xf
	v_mov_b32_dpp v69, v143 quad_perm:[3,3,3,3] row_mask:0xf bank_mask:0xf
	s_nop 0
	v_perm_b32 v70, v67, v66, v136
	v_perm_b32 v71, v69, v68, v137
	v_or_b32_e32 v72, v70, v71
	global_store_dword v[80:81], v72, off offset:3072
	s_nop 0
	s_nop 0
	s_and_b64 vcc, exec, s[28:29]
	s_cbranch_vccnz .LBB0_1718
